# baseline (speedup 1.0000x reference)
.LBB3_33:
	s_waitcnt lgkmcnt(0)
	s_barrier
	s_add_i32 s60, s45, 16
	s_and_b32 s60, s60, 28
	s_or_b32 s60, s60, 2
	s_lshl_b32 s60, s60, 15
	s_or_b32 s61, s60, 0x4000
	s_mov_b32 m0, s38
	s_nop 0
	buffer_load_dwordx4 v166, s[12:15], s61 offen lds
	s_or_b32 s61, s60, 0x6000
	s_mov_b32 m0, s39
	s_nop 0
	buffer_load_dwordx4 v166, s[12:15], s61 offen lds
	s_or_b32 s61, s60, 0xc000
	s_mov_b32 m0, s40
	s_nop 0
	buffer_load_dwordx4 v166, s[12:15], s61 offen lds
	s_or_b32 s61, s60, 0xe000
	s_mov_b32 m0, s42
	s_nop 0
	buffer_load_dwordx4 v166, s[12:15], s61 offen lds
	s_lshr_b32 s62, s21, 1
	s_lshr_b32 s63, s20, 2
	s_xor_b32 s62, s62, s63
	s_and_b32 s62, s62, 1
	s_lshl_b32 s63, s62, 16
	v_add_u32_e32 v232, s63, v168
	v_add_u32_e32 v233, 0x8000, v232
	s_add_i32 s63, s45, 16
	s_and_b32 s63, s63, 28
	s_lshl_b32 s64, s62, 1
	s_or_b32 s63, s63, s64
	s_add_i32 s63, s63, s41
	s_lshl_b32 s63, s63, 1
	v_mov_b32_e32 v234, s63
	s_or_b32 s63, s63, 1
	v_mov_b32_e32 v235, s63
	s_lshl_b32 s64, s62, 8
	s_add_i32 s64, s64, s47
	s_add_i32 s64, s64, 0x20600
	v_lshl_add_u32 v236, v167, 2, s64
	s_waitcnt vmcnt(4)
	s_barrier
	s_movk_i32 s65, 0xffc0
	s_movk_i32 s66, 0xff80
	s_brev_b32 s67, -2
	s_add_i32 s68, s45, 12
	s_and_b32 s68, s68, 28
	s_or_b32 s68, s68, 2
	s_add_i32 s68, s68, s41
	s_lshl_b32 s68, s68, 1
	v_mov_b32_e32 v176, s68
	s_or_b32 s68, s68, 1
	v_mov_b32_e32 v177, s68
	s_add_i32 s68, s47, 0x20500
	v_lshl_add_u32 v182, v167, 2, s68
	ds_read_b128 v[144:147], v232 offset:0
	ds_read_b128 v[148:151], v232 offset:256
	ds_read_b128 v[152:155], v232 offset:2048
	ds_read_b128 v[156:159], v232 offset:2304
	ds_read_b128 v[224:227], v232 offset:4096
	s_waitcnt lgkmcnt(4)
	v_mfma_f32_16x16x32_bf16 v[208:211], v[0:3], v[144:147], 0
	v_mfma_f32_16x16x32_bf16 v[212:215], v[4:7], v[144:147], 0
	ds_read_b128 v[228:231], v232 offset:4352
	s_waitcnt lgkmcnt(4)
	v_mfma_f32_16x16x32_bf16 v[216:219], v[0:3], v[148:151], 0
	v_mfma_f32_16x16x32_bf16 v[220:223], v[4:7], v[148:151], 0
	ds_read_b128 v[144:147], v232 offset:6144
	s_waitcnt lgkmcnt(4)
	v_mfma_f32_16x16x32_bf16 v[208:211], v[8:11], v[152:155], v[208:211]
	v_mfma_f32_16x16x32_bf16 v[212:215], v[12:15], v[152:155], v[212:215]
	ds_read_b128 v[148:151], v232 offset:6400
	v_and_or_b32 v180, v136, s65, v176
	v_and_or_b32 v181, v140, s65, v177
	v_max3_f32 v161, v161, v180, v181
	v_and_b32_e32 v178, 0xffffff80, v136
	v_and_b32_e32 v179, 0xffffff80, v140
	s_waitcnt lgkmcnt(4)
	v_mfma_f32_16x16x32_bf16 v[216:219], v[8:11], v[156:159], v[216:219]
	v_mfma_f32_16x16x32_bf16 v[220:223], v[12:15], v[156:159], v[220:223]
	ds_read_b128 v[152:155], v232 offset:8192
	v_and_or_b32 v180, v137, s65, v176
	v_and_or_b32 v181, v141, s65, v177
	v_max3_f32 v160, v160, v180, v181
	v_and_or_b32 v180, v137, s66, 1
	v_and_or_b32 v181, v141, s66, 1
	v_max_f32_e32 v178, v178, v180
	v_max_f32_e32 v179, v179, v181
	s_waitcnt lgkmcnt(4)
	v_mfma_f32_16x16x32_bf16 v[208:211], v[16:19], v[224:227], v[208:211]
	v_mfma_f32_16x16x32_bf16 v[212:215], v[20:23], v[224:227], v[212:215]
	ds_read_b128 v[156:159], v232 offset:8448
	v_and_or_b32 v180, v138, s65, v176
	v_and_or_b32 v181, v142, s65, v177
	v_max3_f32 v162, v162, v180, v181
	v_and_or_b32 v180, v138, s66, 2
	v_and_or_b32 v181, v142, s66, 2
	v_max_f32_e32 v178, v178, v180
	v_max_f32_e32 v179, v179, v181
	s_waitcnt lgkmcnt(4)
	v_mfma_f32_16x16x32_bf16 v[216:219], v[16:19], v[228:231], v[216:219]
	v_mfma_f32_16x16x32_bf16 v[220:223], v[20:23], v[228:231], v[220:223]
	ds_read_b128 v[224:227], v232 offset:10240
	v_and_or_b32 v180, v139, s65, v176
	v_and_or_b32 v181, v143, s65, v177
	v_max3_f32 v163, v163, v180, v181
	v_and_or_b32 v180, v139, s66, 3
	v_and_or_b32 v181, v143, s66, 3
	v_max_f32_e32 v178, v178, v180
	v_max_f32_e32 v179, v179, v181
	s_waitcnt lgkmcnt(4)
	v_mfma_f32_16x16x32_bf16 v[208:211], v[24:27], v[144:147], v[208:211]
	v_mfma_f32_16x16x32_bf16 v[212:215], v[28:31], v[144:147], v[212:215]
	ds_read_b128 v[228:231], v232 offset:10496
	v_and_or_b32 v180, v128, s65, v176
	v_and_or_b32 v181, v132, s65, v177
	v_max3_f32 v203, v203, v180, v181
	v_and_or_b32 v180, v128, s66, 4
	v_and_or_b32 v181, v132, s66, 4
	v_max_f32_e32 v178, v178, v180
	v_max_f32_e32 v179, v179, v181
	s_waitcnt lgkmcnt(4)
	v_mfma_f32_16x16x32_bf16 v[216:219], v[24:27], v[148:151], v[216:219]
	v_mfma_f32_16x16x32_bf16 v[220:223], v[28:31], v[148:151], v[220:223]
	ds_read_b128 v[144:147], v232 offset:12288
	v_and_or_b32 v180, v129, s65, v176
	v_and_or_b32 v181, v133, s65, v177
	v_max3_f32 v204, v204, v180, v181
	v_and_or_b32 v180, v129, s66, 5
	v_and_or_b32 v181, v133, s66, 5
	v_max_f32_e32 v178, v178, v180
	v_max_f32_e32 v179, v179, v181
	s_waitcnt lgkmcnt(4)
	v_mfma_f32_16x16x32_bf16 v[208:211], v[32:35], v[152:155], v[208:211]
	v_mfma_f32_16x16x32_bf16 v[212:215], v[36:39], v[152:155], v[212:215]
	ds_read_b128 v[148:151], v232 offset:12544
	v_and_or_b32 v180, v130, s65, v176
	v_and_or_b32 v181, v134, s65, v177
	v_max3_f32 v205, v205, v180, v181
	v_and_or_b32 v180, v130, s66, 6
	v_and_or_b32 v181, v134, s66, 6
	v_max_f32_e32 v178, v178, v180
	v_max_f32_e32 v179, v179, v181
	s_waitcnt lgkmcnt(4)
	v_mfma_f32_16x16x32_bf16 v[216:219], v[32:35], v[156:159], v[216:219]
	v_mfma_f32_16x16x32_bf16 v[220:223], v[36:39], v[156:159], v[220:223]
	ds_read_b128 v[152:155], v232 offset:14336
	v_and_or_b32 v180, v131, s65, v176
	v_and_or_b32 v181, v135, s65, v177
	v_max3_f32 v206, v206, v180, v181
	v_and_or_b32 v180, v131, s66, 7
	v_and_or_b32 v181, v135, s66, 7
	v_max_f32_e32 v178, v178, v180
	v_max_f32_e32 v179, v179, v181
	s_waitcnt lgkmcnt(4)
	v_mfma_f32_16x16x32_bf16 v[208:211], v[40:43], v[224:227], v[208:211]
	v_mfma_f32_16x16x32_bf16 v[212:215], v[44:47], v[224:227], v[212:215]
	ds_read_b128 v[156:159], v232 offset:14592
	v_or_b32_e32 v183, v173, v178
	v_ashrrev_i32_e32 v180, 31, v178
	v_bitop3_b32 v183, v180, v183, s67 bitop3:0x6c
	v_or_b32_e32 v184, v173, v179
	v_ashrrev_i32_e32 v181, 31, v179
	v_bitop3_b32 v184, v181, v184, s67 bitop3:0x6c
	s_waitcnt lgkmcnt(4)
	v_mfma_f32_16x16x32_bf16 v[216:219], v[40:43], v[228:231], v[216:219]
	v_mfma_f32_16x16x32_bf16 v[220:223], v[44:47], v[228:231], v[220:223]
	s_waitcnt lgkmcnt(3)
	v_mfma_f32_16x16x32_bf16 v[208:211], v[48:51], v[144:147], v[208:211]
	v_mfma_f32_16x16x32_bf16 v[212:215], v[52:55], v[144:147], v[212:215]
	s_waitcnt lgkmcnt(2)
	v_mfma_f32_16x16x32_bf16 v[216:219], v[48:51], v[148:151], v[216:219]
	v_mfma_f32_16x16x32_bf16 v[220:223], v[52:55], v[148:151], v[220:223]
	s_waitcnt lgkmcnt(1)
	v_mfma_f32_16x16x32_bf16 v[208:211], v[56:59], v[152:155], v[208:211]
	v_mfma_f32_16x16x32_bf16 v[212:215], v[60:63], v[152:155], v[212:215]
	s_waitcnt lgkmcnt(0)
	v_mfma_f32_16x16x32_bf16 v[216:219], v[56:59], v[156:159], v[216:219]
	v_mfma_f32_16x16x32_bf16 v[220:223], v[60:63], v[156:159], v[220:223]
	s_waitcnt vmcnt(0)
	s_barrier
	ds_read_b128 v[144:147], v233 offset:0
	ds_read_b128 v[148:151], v233 offset:256
	ds_read_b128 v[152:155], v233 offset:2048
	ds_read_b128 v[156:159], v233 offset:2304
	ds_read_b128 v[224:227], v233 offset:4096
	s_waitcnt lgkmcnt(4)
	v_mfma_f32_16x16x32_bf16 v[208:211], v[64:67], v[144:147], v[208:211]
	v_mfma_f32_16x16x32_bf16 v[212:215], v[68:71], v[144:147], v[212:215]
	ds_read_b128 v[228:231], v233 offset:4352
	s_waitcnt lgkmcnt(4)
	v_mfma_f32_16x16x32_bf16 v[216:219], v[64:67], v[148:151], v[216:219]
	v_mfma_f32_16x16x32_bf16 v[220:223], v[68:71], v[148:151], v[220:223]
	ds_read_b128 v[144:147], v233 offset:6144
	s_waitcnt lgkmcnt(4)
	v_mfma_f32_16x16x32_bf16 v[208:211], v[72:75], v[152:155], v[208:211]
	v_mfma_f32_16x16x32_bf16 v[212:215], v[76:79], v[152:155], v[212:215]
	ds_read_b128 v[148:151], v233 offset:6400
	s_waitcnt lgkmcnt(4)
	v_mfma_f32_16x16x32_bf16 v[216:219], v[72:75], v[156:159], v[216:219]
	v_mfma_f32_16x16x32_bf16 v[220:223], v[76:79], v[156:159], v[220:223]
	ds_read_b128 v[152:155], v233 offset:8192
	s_waitcnt lgkmcnt(4)
	v_mfma_f32_16x16x32_bf16 v[208:211], v[80:83], v[224:227], v[208:211]
	v_mfma_f32_16x16x32_bf16 v[212:215], v[84:87], v[224:227], v[212:215]
	ds_read_b128 v[156:159], v233 offset:8448
	s_waitcnt lgkmcnt(4)
	v_mfma_f32_16x16x32_bf16 v[216:219], v[80:83], v[228:231], v[216:219]
	v_mfma_f32_16x16x32_bf16 v[220:223], v[84:87], v[228:231], v[220:223]
	ds_read_b128 v[224:227], v233 offset:10240
	s_waitcnt lgkmcnt(4)
	v_mfma_f32_16x16x32_bf16 v[208:211], v[88:91], v[144:147], v[208:211]
	v_mfma_f32_16x16x32_bf16 v[212:215], v[92:95], v[144:147], v[212:215]
	ds_read_b128 v[228:231], v233 offset:10496
	s_waitcnt lgkmcnt(4)
	v_mfma_f32_16x16x32_bf16 v[216:219], v[88:91], v[148:151], v[216:219]
	v_mfma_f32_16x16x32_bf16 v[220:223], v[92:95], v[148:151], v[220:223]
	ds_read_b128 v[144:147], v233 offset:12288
	s_waitcnt lgkmcnt(4)
	v_mfma_f32_16x16x32_bf16 v[208:211], v[96:99], v[152:155], v[208:211]
	v_mfma_f32_16x16x32_bf16 v[212:215], v[100:103], v[152:155], v[212:215]
	ds_read_b128 v[148:151], v233 offset:12544
	s_waitcnt lgkmcnt(4)
	v_mfma_f32_16x16x32_bf16 v[216:219], v[96:99], v[156:159], v[216:219]
	v_mfma_f32_16x16x32_bf16 v[220:223], v[100:103], v[156:159], v[220:223]
	ds_read_b128 v[152:155], v233 offset:14336
	s_waitcnt lgkmcnt(4)
	v_mfma_f32_16x16x32_bf16 v[208:211], v[104:107], v[224:227], v[208:211]
	v_mfma_f32_16x16x32_bf16 v[212:215], v[108:111], v[224:227], v[212:215]
	ds_read_b128 v[156:159], v233 offset:14592
	s_waitcnt lgkmcnt(4)
	v_mfma_f32_16x16x32_bf16 v[216:219], v[104:107], v[228:231], v[216:219]
	v_mfma_f32_16x16x32_bf16 v[220:223], v[108:111], v[228:231], v[220:223]
	s_waitcnt lgkmcnt(3)
	v_mfma_f32_16x16x32_bf16 v[208:211], v[112:115], v[144:147], v[208:211]
	v_mfma_f32_16x16x32_bf16 v[212:215], v[116:119], v[144:147], v[212:215]
	s_waitcnt lgkmcnt(2)
	v_mfma_f32_16x16x32_bf16 v[216:219], v[112:115], v[148:151], v[216:219]
	v_mfma_f32_16x16x32_bf16 v[220:223], v[116:119], v[148:151], v[220:223]
	s_waitcnt lgkmcnt(1)
	v_mfma_f32_16x16x32_bf16 v[208:211], v[120:123], v[152:155], v[208:211]
	v_mfma_f32_16x16x32_bf16 v[212:215], v[124:127], v[152:155], v[212:215]
	s_waitcnt lgkmcnt(0)
	v_mfma_f32_16x16x32_bf16 v[216:219], v[120:123], v[156:159], v[216:219]
	v_mfma_f32_16x16x32_bf16 v[220:223], v[124:127], v[156:159], v[220:223]
	s_nop 7
	s_nop 3
	v_and_or_b32 v237, v208, s65, v234
	v_and_or_b32 v238, v216, s65, v235
	v_max3_f32 v161, v161, v237, v238
	v_and_b32_e32 v174, 0xffffff80, v208
	v_and_b32_e32 v175, 0xffffff80, v216
	v_and_or_b32 v237, v209, s65, v234
	v_and_or_b32 v238, v217, s65, v235
	v_max3_f32 v160, v160, v237, v238
	v_and_or_b32 v237, v209, s66, 1
	v_and_or_b32 v238, v217, s66, 1
	v_max_f32_e32 v174, v174, v237
	v_max_f32_e32 v175, v175, v238
	v_and_or_b32 v237, v210, s65, v234
	v_and_or_b32 v238, v218, s65, v235
	v_max3_f32 v162, v162, v237, v238
	v_and_or_b32 v237, v210, s66, 2
	v_and_or_b32 v238, v218, s66, 2
	v_max_f32_e32 v174, v174, v237
	v_max_f32_e32 v175, v175, v238
	v_and_or_b32 v237, v211, s65, v234
	v_and_or_b32 v238, v219, s65, v235
	v_max3_f32 v163, v163, v237, v238
	v_and_or_b32 v237, v211, s66, 3
	v_and_or_b32 v238, v219, s66, 3
	v_max_f32_e32 v174, v174, v237
	v_max_f32_e32 v175, v175, v238
	v_and_or_b32 v237, v212, s65, v234
	v_and_or_b32 v238, v220, s65, v235
	v_max3_f32 v203, v203, v237, v238
	v_and_or_b32 v237, v212, s66, 4
	v_and_or_b32 v238, v220, s66, 4
	v_max_f32_e32 v174, v174, v237
	v_max_f32_e32 v175, v175, v238
	v_and_or_b32 v237, v213, s65, v234
	v_and_or_b32 v238, v221, s65, v235
	v_max3_f32 v204, v204, v237, v238
	v_and_or_b32 v237, v213, s66, 5
	v_and_or_b32 v238, v221, s66, 5
	v_max_f32_e32 v174, v174, v237
	v_max_f32_e32 v175, v175, v238
	v_and_or_b32 v237, v214, s65, v234
	v_and_or_b32 v238, v222, s65, v235
	v_max3_f32 v205, v205, v237, v238
	v_and_or_b32 v237, v214, s66, 6
	v_and_or_b32 v238, v222, s66, 6
	v_max_f32_e32 v174, v174, v237
	v_max_f32_e32 v175, v175, v238
	v_and_or_b32 v237, v215, s65, v234
	v_and_or_b32 v238, v223, s65, v235
	v_max3_f32 v206, v206, v237, v238
	v_and_or_b32 v237, v215, s66, 7
	v_and_or_b32 v238, v223, s66, 7
	v_max_f32_e32 v174, v174, v237
	v_max_f32_e32 v175, v175, v238
	v_or_b32_e32 v237, v173, v174
	v_ashrrev_i32_e32 v238, 31, v174
	v_bitop3_b32 v237, v238, v237, s67 bitop3:0x6c
	ds_max_i32 v236, v237
	v_or_b32_e32 v237, v173, v175
	v_ashrrev_i32_e32 v238, 31, v175
	v_bitop3_b32 v237, v238, v237, s67 bitop3:0x6c
	ds_max_i32 v236, v237 offset:64
	ds_max_i32 v182, v183
	ds_max_i32 v182, v184 offset:64
	v_mov_b32_e32 v0, v161
	v_mov_b32_e32 v1, v160
	v_mov_b32_e32 v3, v162
	v_mov_b32_e32 v4, v163
	v_mov_b32_e32 v5, v203
	v_mov_b32_e32 v6, v204
	v_mov_b32_e32 v7, v205
	v_mov_b32_e32 v8, v206
	s_movk_i32 s2, 0xff80
	s_brev_b32 s3, -2
	v_mbcnt_lo_u32_b32 v2, -1, 0
	s_andn2_b32 s23, s23, 63
	s_lshl_b64 s[0:1], s[16:17], 13
	s_waitcnt vmcnt(0)
	v_mbcnt_hi_u32_b32 v2, -1, v2
	s_add_u32 s4, s10, s0
	v_add_u32_e32 v9, s23, v2
	s_addc_u32 s5, s11, s1
	s_mov_b32 s6, 4
	s_lshl_b32 s0, s6, 7
	v_cmp_gt_i32_e32 vcc, s0, v9
	s_waitcnt lgkmcnt(0)
	s_barrier
	s_and_saveexec_b64 s[0:1], vcc
	s_cbranch_execz .LBB3_35
	v_mov_b32_e32 v10, 0x20000
	v_lshl_add_u32 v10, v9, 2, v10
	ds_read_b32 v10, v10
	s_movk_i32 s6, 0x63
	v_and_b32_e32 v12, 0x7f, v9
	s_waitcnt lgkmcnt(0)
	v_ashrrev_i32_e32 v11, 31, v10
	v_and_b32_e32 v13, 0x7fffffff, v11
	v_bitop3_b32 v11, v11, v10, s3 bitop3:0x6c
	v_lshlrev_b32_e32 v14, 2, v11
	v_and_b32_e32 v14, 16, v14
	s_lshl_b32 s3, s20, 7
	v_bitop3_b32 v13, v13, s6, v10 bitop3:0x48
	v_or3_b32 v13, v13, s3, v14
	v_bfrev_b32_e32 v14, 1
	v_cmp_lt_i32_e32 vcc, -1, v10
	v_lshrrev_b32_e32 v15, 1, v11
	v_and_b32_e32 v15, 12, v15
	v_cndmask_b32_e32 v10, -1, v14, vcc
	v_bitop3_b32 v11, v11, v10, s2 bitop3:0x6c
	s_movk_i32 s2, 0x3ff
	v_bitop3_b32 v10, v13, s2, v15 bitop3:0x36
	s_lshl_b32 s2, s22, 7
	s_addk_i32 s2, 0x80
	v_add_u32_e32 v9, s2, v9
	s_movk_i32 s2, 0x380
	v_and_or_b32 v9, v9, s2, v12
	v_lshlrev_b32_e32 v9, 3, v9
	global_atomic_umax_x2 v9, v[10:11], s[4:5]
